# L2 prefetch (two sc1 dword loads per K-loop trip, 2 K-tiles ahead of the LDS-DMA) in the GLA out-projection GEMM K-loop; waits recounted
# baseline (speedup 1.0000x reference)
.LBB0_689:
	s_cmp_lt_i32 s46, 7
	s_cselect_b64 s[2:3], -1, 0
	s_and_b64 s[12:13], s[2:3], s[6:7]
	s_andn2_b64 vcc, exec, s[12:13]
	s_cbranch_vccnz .LBB0_738
	s_mov_b64 s[2:3], s[0:1]
	v_lshrrev_b32_e32 v254, 6, v0
	v_and_b32_e32 v253, 31, v0
	v_lshl_or_b32 v254, v254, 5, v253
	v_bfe_u32 v253, v0, 5, 1
	v_lshlrev_b32_e32 v254, 12, v254
	v_lshl_or_b32 v254, v253, 7, v254
	s_cmpk_lt_i32 s96, 0x400
	s_load_dwordx2 s[8:9], s[2:3], 0xc8
	s_cselect_b64 s[6:7], -1, 0
	s_cmpk_gt_i32 s96, 0x3ff
	v_readfirstlane_b32 s2, v0
	s_waitcnt lgkmcnt(0)
	s_cbranch_scc1 .LBB0_696
	s_ashr_i32 s3, s96, 31
	s_lshr_b32 s3, s3, 29
	s_add_i32 s3, s96, s3
	s_and_b32 s4, s3, -8
	s_sub_i32 s4, s96, s4
	s_cmp_gt_i32 s4, -1
	s_cbranch_scc0 .LBB0_693
	s_lshl_b32 s5, s4, 7
	s_cbranch_execz .LBB0_694
	s_branch .LBB0_695

.LBB0_712:
	ds_read_b128 v[140:143], v205
	ds_read_b128 v[144:147], v205 offset:1024
	ds_read_b128 v[148:151], v205 offset:2048
	ds_read_b128 v[152:155], v205 offset:3072
	ds_read_b128 v[182:185], v207
	ds_read_b128 v[186:189], v207 offset:1024
	ds_read_b128 v[196:199], v207 offset:2048
	ds_read_b128 v[212:215], v207 offset:3072
	s_mov_b64 s[72:73], s[56:57]
	s_add_u32 s2, s69, s72
	s_addc_u32 s74, s70, s73
	s_add_u32 s56, s72, 0x100
	s_addc_u32 s57, s73, 0
	s_cmpk_eq_i32 s72, 0xf00
	s_cselect_b64 s[58:59], -1, 0
	s_and_b64 s[60:61], s[58:59], exec
	s_cselect_b32 s61, s35, s74
	s_cselect_b32 s60, s68, s2
	s_cselect_b32 s2, 0, s56
	v_lshl_add_u64 v[4:5], v[136:137], 0, s[72:73]
	s_add_i32 m0, s42, 0xc000
	ds_read_b128 v[216:219], v210
	ds_read_b128 v[220:223], v210 offset:1024
	ds_read_b128 v[224:227], v210 offset:2048
	ds_read_b128 v[228:231], v210 offset:3072
	ds_read_b128 v[232:235], v210 offset:4096
	ds_read_b128 v[236:239], v210 offset:5120
	ds_read_b128 v[244:247], v210 offset:6144
	ds_read_b128 v[248:251], v210 offset:7168
	global_load_lds_dwordx4 v[4:5], off
	v_lshl_add_u64 v[4:5], v[134:135], 0, s[72:73]
	s_add_i32 m0, s42, 0xe000
	s_nop 0
	global_load_lds_dwordx4 v[4:5], off
	s_waitcnt vmcnt(8)
	s_waitcnt lgkmcnt(0)
	s_barrier
	s_setprio 1
	s_waitcnt lgkmcnt(0)
	v_mfma_f32_16x16x32_bf16 v[130:133], v[140:143], v[216:219], v[130:133]
	v_mfma_f32_16x16x32_bf16 v[126:129], v[148:151], v[216:219], v[126:129]
	v_mfma_f32_16x16x32_bf16 v[114:117], v[140:143], v[224:227], v[114:117]
	v_mfma_f32_16x16x32_bf16 v[110:113], v[148:151], v[224:227], v[110:113]
	v_mfma_f32_16x16x32_bf16 v[98:101], v[140:143], v[232:235], v[98:101]
	v_mfma_f32_16x16x32_bf16 v[94:97], v[148:151], v[232:235], v[94:97]
	v_mfma_f32_16x16x32_bf16 v[82:85], v[140:143], v[244:247], v[82:85]
	v_mfma_f32_16x16x32_bf16 v[78:81], v[148:151], v[244:247], v[78:81]
	v_mfma_f32_16x16x32_bf16 v[130:133], v[144:147], v[220:223], v[130:133]
	v_mfma_f32_16x16x32_bf16 v[126:129], v[152:155], v[220:223], v[126:129]
	v_mfma_f32_16x16x32_bf16 v[114:117], v[144:147], v[228:231], v[114:117]
	v_mfma_f32_16x16x32_bf16 v[110:113], v[152:155], v[228:231], v[110:113]
	v_mfma_f32_16x16x32_bf16 v[98:101], v[144:147], v[236:239], v[98:101]
	v_mfma_f32_16x16x32_bf16 v[94:97], v[152:155], v[236:239], v[94:97]
	v_mfma_f32_16x16x32_bf16 v[82:85], v[144:147], v[248:251], v[82:85]
	v_mfma_f32_16x16x32_bf16 v[78:81], v[152:155], v[248:251], v[78:81]
	s_setprio 0
	s_setprio 1
	v_mfma_f32_16x16x32_bf16 v[122:125], v[182:185], v[216:219], v[122:125]
	v_mfma_f32_16x16x32_bf16 v[118:121], v[196:199], v[216:219], v[118:121]
	v_mfma_f32_16x16x32_bf16 v[106:109], v[182:185], v[224:227], v[106:109]
	v_mfma_f32_16x16x32_bf16 v[102:105], v[196:199], v[224:227], v[102:105]
	v_mfma_f32_16x16x32_bf16 v[90:93], v[182:185], v[232:235], v[90:93]
	v_mfma_f32_16x16x32_bf16 v[86:89], v[196:199], v[232:235], v[86:89]
	v_mfma_f32_16x16x32_bf16 v[74:77], v[182:185], v[244:247], v[74:77]
	v_mfma_f32_16x16x32_bf16 v[70:73], v[196:199], v[244:247], v[70:73]
	v_mfma_f32_16x16x32_bf16 v[122:125], v[186:189], v[220:223], v[122:125]
	v_mfma_f32_16x16x32_bf16 v[118:121], v[212:215], v[220:223], v[118:121]
	v_mfma_f32_16x16x32_bf16 v[106:109], v[186:189], v[228:231], v[106:109]
	v_mfma_f32_16x16x32_bf16 v[102:105], v[212:215], v[228:231], v[102:105]
	v_mfma_f32_16x16x32_bf16 v[90:93], v[186:189], v[236:239], v[90:93]
	v_mfma_f32_16x16x32_bf16 v[86:89], v[212:215], v[236:239], v[86:89]
	v_mfma_f32_16x16x32_bf16 v[74:77], v[186:189], v[248:251], v[74:77]
	v_mfma_f32_16x16x32_bf16 v[70:73], v[212:215], v[248:251], v[70:73]
	s_setprio 0
	s_barrier
	s_add_i32 s72, s63, s15
	v_lshl_add_u64 v[156:157], s[60:61], 0, v[160:161]
	s_mov_b32 m0, s72
	ds_read_b128 v[216:219], v210 offset:16384
	ds_read_b128 v[220:223], v210 offset:17408
	ds_read_b128 v[224:227], v210 offset:18432
	ds_read_b128 v[228:231], v210 offset:19456
	ds_read_b128 v[232:235], v210 offset:20480
	ds_read_b128 v[236:239], v210 offset:21504
	ds_read_b128 v[244:247], v210 offset:22528
	ds_read_b128 v[248:251], v210 offset:23552
	global_load_lds_dwordx4 v[156:157], off
	s_add_i32 m0, s72, 0x2000
	s_add_u32 s72, s60, 0x80000
	v_lshl_add_u64 v[178:179], s[60:61], 0, v[164:165]
	s_addc_u32 s73, s61, 0
	s_add_i32 s74, s64, s15
	global_load_lds_dwordx4 v[178:179], off
	v_lshl_add_u64 v[4:5], s[72:73], 0, v[160:161]
	s_mov_b32 m0, s74
	s_nop 0
	global_load_lds_dwordx4 v[4:5], off
	v_lshl_add_u64 v[4:5], s[72:73], 0, v[164:165]
	s_add_i32 m0, s74, 0x2000
	s_and_b64 s[72:73], s[10:11], s[58:59]
	s_and_b64 s[72:73], s[72:73], exec
	s_cselect_b32 s72, s38, s54
	s_cselect_b32 s73, s39, s55
	s_add_u32 s72, s72, s2
	s_addc_u32 s73, s73, 0
	global_load_lds_dwordx4 v[4:5], off
	v_lshl_add_u64 v[192:193], s[72:73], 0, v[158:159]
	s_mov_b32 m0, s42
	v_lshl_add_u64 v[202:203], s[72:73], 0, v[162:163]
	global_load_lds_dwordx4 v[192:193], off
	s_mov_b32 m0, s43
	s_nop 0
	global_load_lds_dwordx4 v[202:203], off
	s_waitcnt vmcnt(8)
	global_load_dword v253, v254, s[72:73] offset:256 sc1
	global_load_dword v253, v254, s[60:61] offset:256 sc1
	s_waitcnt lgkmcnt(0)
	s_barrier
	s_setprio 1
	s_waitcnt lgkmcnt(0)
	v_mfma_f32_16x16x32_bf16 v[66:69], v[140:143], v[216:219], v[66:69]
	v_mfma_f32_16x16x32_bf16 v[62:65], v[148:151], v[216:219], v[62:65]
	v_mfma_f32_16x16x32_bf16 v[50:53], v[140:143], v[224:227], v[50:53]
	v_mfma_f32_16x16x32_bf16 v[46:49], v[148:151], v[224:227], v[46:49]
	v_mfma_f32_16x16x32_bf16 v[34:37], v[140:143], v[232:235], v[34:37]
	v_mfma_f32_16x16x32_bf16 v[30:33], v[148:151], v[232:235], v[30:33]
	v_mfma_f32_16x16x32_bf16 v[18:21], v[140:143], v[244:247], v[18:21]
	v_mfma_f32_16x16x32_bf16 v[14:17], v[148:151], v[244:247], v[14:17]
	v_mfma_f32_16x16x32_bf16 v[66:69], v[144:147], v[220:223], v[66:69]
	v_mfma_f32_16x16x32_bf16 v[62:65], v[152:155], v[220:223], v[62:65]
	v_mfma_f32_16x16x32_bf16 v[50:53], v[144:147], v[228:231], v[50:53]
	v_mfma_f32_16x16x32_bf16 v[46:49], v[152:155], v[228:231], v[46:49]
	v_mfma_f32_16x16x32_bf16 v[34:37], v[144:147], v[236:239], v[34:37]
	v_mfma_f32_16x16x32_bf16 v[30:33], v[152:155], v[236:239], v[30:33]
	v_mfma_f32_16x16x32_bf16 v[18:21], v[144:147], v[248:251], v[18:21]
	v_mfma_f32_16x16x32_bf16 v[14:17], v[152:155], v[248:251], v[14:17]
	s_setprio 0
	s_setprio 1
	v_mfma_f32_16x16x32_bf16 v[58:61], v[182:185], v[216:219], v[58:61]
	v_mfma_f32_16x16x32_bf16 v[54:57], v[196:199], v[216:219], v[54:57]
	v_mfma_f32_16x16x32_bf16 v[42:45], v[182:185], v[224:227], v[42:45]
	v_mfma_f32_16x16x32_bf16 v[38:41], v[196:199], v[224:227], v[38:41]
	v_mfma_f32_16x16x32_bf16 v[26:29], v[182:185], v[232:235], v[26:29]
	v_mfma_f32_16x16x32_bf16 v[22:25], v[196:199], v[232:235], v[22:25]
	v_mfma_f32_16x16x32_bf16 v[10:13], v[182:185], v[244:247], v[10:13]
	v_mfma_f32_16x16x32_bf16 v[4:7], v[196:199], v[244:247], v[6:9]
	v_mfma_f32_16x16x32_bf16 v[58:61], v[186:189], v[220:223], v[58:61]
	v_mfma_f32_16x16x32_bf16 v[54:57], v[212:215], v[220:223], v[54:57]
	v_mfma_f32_16x16x32_bf16 v[42:45], v[186:189], v[228:231], v[42:45]
	v_mfma_f32_16x16x32_bf16 v[38:41], v[212:215], v[228:231], v[38:41]
	v_mfma_f32_16x16x32_bf16 v[26:29], v[186:189], v[236:239], v[26:29]
	v_mfma_f32_16x16x32_bf16 v[22:25], v[212:215], v[236:239], v[22:25]
	v_mfma_f32_16x16x32_bf16 v[10:13], v[186:189], v[248:251], v[10:13]
	v_mfma_f32_16x16x32_bf16 v[4:7], v[212:215], v[248:251], v[4:7]
	s_setprio 0
	s_barrier
	s_add_i32 s2, 0, 0x18000
	v_add_u32_e32 v3, s2, v177
	s_add_i32 s74, 0, 0x1c000
	ds_read_b128 v[140:143], v3
	ds_read_b128 v[144:147], v3 offset:1024
	ds_read_b128 v[148:151], v3 offset:2048
	ds_read_b128 v[152:155], v3 offset:3072
	v_add_u32_e32 v3, s74, v177
	ds_read_b128 v[182:185], v3
	ds_read_b128 v[186:189], v3 offset:1024
	ds_read_b128 v[196:199], v3 offset:2048
	ds_read_b128 v[212:215], v3 offset:3072
	s_add_u32 s72, s72, 0x80000
	s_addc_u32 s73, s73, 0
	s_mov_b32 m0, s48
	v_lshl_add_u64 v[8:9], s[72:73], 0, v[158:159]
	ds_read_b128 v[216:219], v210 offset:32768
	ds_read_b128 v[220:223], v210 offset:33792
	ds_read_b128 v[224:227], v210 offset:34816
	ds_read_b128 v[228:231], v210 offset:35840
	ds_read_b128 v[232:235], v210 offset:36864
	ds_read_b128 v[236:239], v210 offset:37888
	ds_read_b128 v[244:247], v210 offset:38912
	ds_read_b128 v[248:251], v210 offset:39936
	global_load_lds_dwordx4 v[8:9], off
	v_lshl_add_u64 v[8:9], s[72:73], 0, v[162:163]
	s_mov_b32 m0, s49
	s_nop 0
	global_load_lds_dwordx4 v[8:9], off
	s_waitcnt vmcnt(10)
	s_waitcnt lgkmcnt(0)
	s_barrier
	s_setprio 1
	s_waitcnt lgkmcnt(0)
	v_mfma_f32_16x16x32_bf16 v[130:133], v[140:143], v[216:219], v[130:133]
	v_mfma_f32_16x16x32_bf16 v[126:129], v[148:151], v[216:219], v[126:129]
	v_mfma_f32_16x16x32_bf16 v[114:117], v[140:143], v[224:227], v[114:117]
	v_mfma_f32_16x16x32_bf16 v[110:113], v[148:151], v[224:227], v[110:113]
	v_mfma_f32_16x16x32_bf16 v[98:101], v[140:143], v[232:235], v[98:101]
	v_mfma_f32_16x16x32_bf16 v[94:97], v[148:151], v[232:235], v[94:97]
	v_mfma_f32_16x16x32_bf16 v[82:85], v[140:143], v[244:247], v[82:85]
	v_mfma_f32_16x16x32_bf16 v[78:81], v[148:151], v[244:247], v[78:81]
	v_mfma_f32_16x16x32_bf16 v[130:133], v[144:147], v[220:223], v[130:133]
	v_mfma_f32_16x16x32_bf16 v[126:129], v[152:155], v[220:223], v[126:129]
	v_mfma_f32_16x16x32_bf16 v[114:117], v[144:147], v[228:231], v[114:117]
	v_mfma_f32_16x16x32_bf16 v[110:113], v[152:155], v[228:231], v[110:113]
	v_mfma_f32_16x16x32_bf16 v[98:101], v[144:147], v[236:239], v[98:101]
	v_mfma_f32_16x16x32_bf16 v[94:97], v[152:155], v[236:239], v[94:97]
	v_mfma_f32_16x16x32_bf16 v[82:85], v[144:147], v[248:251], v[82:85]
	v_mfma_f32_16x16x32_bf16 v[78:81], v[152:155], v[248:251], v[78:81]
	s_setprio 0
	s_setprio 1
	v_mfma_f32_16x16x32_bf16 v[122:125], v[182:185], v[216:219], v[122:125]
	v_mfma_f32_16x16x32_bf16 v[118:121], v[196:199], v[216:219], v[118:121]
	v_mfma_f32_16x16x32_bf16 v[106:109], v[182:185], v[224:227], v[106:109]
	v_mfma_f32_16x16x32_bf16 v[102:105], v[196:199], v[224:227], v[102:105]
	v_mfma_f32_16x16x32_bf16 v[90:93], v[182:185], v[232:235], v[90:93]
	v_mfma_f32_16x16x32_bf16 v[86:89], v[196:199], v[232:235], v[86:89]
	v_mfma_f32_16x16x32_bf16 v[74:77], v[182:185], v[244:247], v[74:77]
	v_mfma_f32_16x16x32_bf16 v[70:73], v[196:199], v[244:247], v[70:73]
	v_mfma_f32_16x16x32_bf16 v[122:125], v[186:189], v[220:223], v[122:125]
	v_mfma_f32_16x16x32_bf16 v[118:121], v[212:215], v[220:223], v[118:121]
	v_mfma_f32_16x16x32_bf16 v[106:109], v[186:189], v[228:231], v[106:109]
	v_mfma_f32_16x16x32_bf16 v[102:105], v[212:215], v[228:231], v[102:105]
	v_mfma_f32_16x16x32_bf16 v[90:93], v[186:189], v[236:239], v[90:93]
	v_mfma_f32_16x16x32_bf16 v[86:89], v[212:215], v[236:239], v[86:89]
	v_mfma_f32_16x16x32_bf16 v[74:77], v[186:189], v[248:251], v[74:77]
	v_mfma_f32_16x16x32_bf16 v[70:73], v[212:215], v[248:251], v[70:73]
	s_setprio 0
	s_barrier
	s_add_i32 s2, s2, s15
	v_lshl_add_u64 v[8:9], v[156:157], 0, s[28:29]
	s_mov_b32 m0, s2
	ds_read_b128 v[216:219], v210 offset:49152
	ds_read_b128 v[220:223], v210 offset:50176
	ds_read_b128 v[224:227], v210 offset:51200
	ds_read_b128 v[228:231], v210 offset:52224
	ds_read_b128 v[232:235], v210 offset:53248
	ds_read_b128 v[236:239], v210 offset:54272
	ds_read_b128 v[244:247], v210 offset:55296
	ds_read_b128 v[248:251], v210 offset:56320
	global_load_lds_dwordx4 v[8:9], off
	s_add_i32 m0, s2, 0x2000
	s_add_u32 s60, s60, 0x80080
	v_lshl_add_u64 v[8:9], v[178:179], 0, s[28:29]
	s_addc_u32 s61, s61, 0
	s_add_i32 s2, s74, s15
	global_load_lds_dwordx4 v[8:9], off
	v_lshl_add_u64 v[8:9], s[60:61], 0, v[160:161]
	s_mov_b32 m0, s2
	s_nop 0
	global_load_lds_dwordx4 v[8:9], off
	v_lshl_add_u64 v[8:9], s[60:61], 0, v[164:165]
	s_add_i32 m0, s2, 0x2000
	s_nop 0
	global_load_lds_dwordx4 v[8:9], off
	v_lshl_add_u64 v[8:9], v[192:193], 0, s[28:29]
	s_mov_b32 m0, s51
	s_nop 0
	global_load_lds_dwordx4 v[8:9], off
	v_lshl_add_u64 v[8:9], v[202:203], 0, s[28:29]
	s_mov_b32 m0, s52
	s_nop 0
	global_load_lds_dwordx4 v[8:9], off
	s_waitcnt vmcnt(10)
	s_waitcnt lgkmcnt(0)
	s_barrier
	s_setprio 1
	s_waitcnt lgkmcnt(0)
	v_mfma_f32_16x16x32_bf16 v[66:69], v[140:143], v[216:219], v[66:69]
	v_mfma_f32_16x16x32_bf16 v[62:65], v[148:151], v[216:219], v[62:65]
	v_mfma_f32_16x16x32_bf16 v[50:53], v[140:143], v[224:227], v[50:53]
	v_mfma_f32_16x16x32_bf16 v[46:49], v[148:151], v[224:227], v[46:49]
	v_mfma_f32_16x16x32_bf16 v[34:37], v[140:143], v[232:235], v[34:37]
	v_mfma_f32_16x16x32_bf16 v[30:33], v[148:151], v[232:235], v[30:33]
	v_mfma_f32_16x16x32_bf16 v[18:21], v[140:143], v[244:247], v[18:21]
	v_mfma_f32_16x16x32_bf16 v[14:17], v[148:151], v[244:247], v[14:17]
	v_mfma_f32_16x16x32_bf16 v[66:69], v[144:147], v[220:223], v[66:69]
	v_mfma_f32_16x16x32_bf16 v[62:65], v[152:155], v[220:223], v[62:65]
	v_mfma_f32_16x16x32_bf16 v[50:53], v[144:147], v[228:231], v[50:53]
	v_mfma_f32_16x16x32_bf16 v[46:49], v[152:155], v[228:231], v[46:49]
	v_mfma_f32_16x16x32_bf16 v[34:37], v[144:147], v[236:239], v[34:37]
	v_mfma_f32_16x16x32_bf16 v[30:33], v[152:155], v[236:239], v[30:33]
	v_mfma_f32_16x16x32_bf16 v[18:21], v[144:147], v[248:251], v[18:21]
	v_mfma_f32_16x16x32_bf16 v[14:17], v[152:155], v[248:251], v[14:17]
	s_setprio 0
	s_setprio 1
	v_mfma_f32_16x16x32_bf16 v[58:61], v[182:185], v[216:219], v[58:61]
	v_mfma_f32_16x16x32_bf16 v[54:57], v[196:199], v[216:219], v[54:57]
	v_mfma_f32_16x16x32_bf16 v[42:45], v[182:185], v[224:227], v[42:45]
	v_mfma_f32_16x16x32_bf16 v[38:41], v[196:199], v[224:227], v[38:41]
	v_mfma_f32_16x16x32_bf16 v[26:29], v[182:185], v[232:235], v[26:29]
	v_mfma_f32_16x16x32_bf16 v[22:25], v[196:199], v[232:235], v[22:25]
	v_mfma_f32_16x16x32_bf16 v[8:11], v[182:185], v[244:247], v[10:13]
	v_mfma_f32_16x16x32_bf16 v[4:7], v[196:199], v[244:247], v[4:7]
	v_mfma_f32_16x16x32_bf16 v[58:61], v[186:189], v[220:223], v[58:61]
	v_mfma_f32_16x16x32_bf16 v[54:57], v[212:215], v[220:223], v[54:57]
	v_mfma_f32_16x16x32_bf16 v[42:45], v[186:189], v[228:231], v[42:45]
	v_mfma_f32_16x16x32_bf16 v[38:41], v[212:215], v[228:231], v[38:41]
	v_mfma_f32_16x16x32_bf16 v[26:29], v[186:189], v[236:239], v[26:29]
	v_mfma_f32_16x16x32_bf16 v[22:25], v[212:215], v[236:239], v[22:25]
	v_mfma_f32_16x16x32_bf16 v[10:13], v[186:189], v[248:251], v[8:11]
	v_mfma_f32_16x16x32_bf16 v[6:9], v[212:215], v[248:251], v[4:7]
	s_setprio 0
	s_barrier
	s_add_i32 s2, s71, 4
	s_and_b32 s2, s2, 6
	s_cmp_lg_u32 s2, 0
	s_cselect_b64 s[60:61], -1, 0
	s_or_b64 s[58:59], s[58:59], s[60:61]
	s_and_b64 vcc, exec, s[58:59]
	s_cbranch_vccnz .LBB0_711
	ds_read2st64_b32 v[4:5], v138 offset1:1
	ds_read2st64_b32 v[140:141], v138 offset0:2 offset1:3
	ds_read2st64_b32 v[142:143], v138 offset0:8 offset1:9
	ds_read2st64_b32 v[144:145], v138 offset0:10 offset1:11
	s_waitcnt lgkmcnt(0)
	v_pk_mul_f32 v[132:133], v[132:133], v[4:5] op_sel_hi:[1,0]
	v_pk_mul_f32 v[130:131], v[130:131], v[4:5] op_sel_hi:[1,0]
	v_pk_mul_f32 v[128:129], v[128:129], v[4:5] op_sel_hi:[1,0]
	v_pk_mul_f32 v[126:127], v[126:127], v[4:5] op_sel_hi:[1,0]
	v_pk_mul_f32 v[124:125], v[124:125], v[4:5] op_sel_hi:[1,0]
	v_pk_mul_f32 v[122:123], v[122:123], v[4:5] op_sel_hi:[1,0]
	v_pk_mul_f32 v[120:121], v[120:121], v[4:5] op_sel_hi:[1,0]
	v_pk_mul_f32 v[118:119], v[118:119], v[4:5] op_sel_hi:[1,0]
	v_mov_b32_e32 v4, v5
	v_pk_mul_f32 v[116:117], v[116:117], v[4:5] op_sel_hi:[1,0]
	v_pk_mul_f32 v[114:115], v[114:115], v[4:5] op_sel_hi:[1,0]
	v_pk_mul_f32 v[112:113], v[112:113], v[4:5] op_sel_hi:[1,0]
	v_pk_mul_f32 v[110:111], v[110:111], v[4:5] op_sel_hi:[1,0]
	v_pk_mul_f32 v[108:109], v[108:109], v[4:5] op_sel_hi:[1,0]
	v_pk_mul_f32 v[106:107], v[106:107], v[4:5] op_sel_hi:[1,0]
	v_pk_mul_f32 v[104:105], v[104:105], v[4:5] op_sel_hi:[1,0]
	v_pk_mul_f32 v[102:103], v[102:103], v[4:5] op_sel_hi:[1,0]
	v_mov_b32_e32 v4, v141
	v_pk_mul_f32 v[84:85], v[84:85], v[4:5] op_sel_hi:[1,0]
	v_pk_mul_f32 v[82:83], v[82:83], v[4:5] op_sel_hi:[1,0]
	v_pk_mul_f32 v[80:81], v[80:81], v[4:5] op_sel_hi:[1,0]
	v_pk_mul_f32 v[78:79], v[78:79], v[4:5] op_sel_hi:[1,0]
	v_pk_mul_f32 v[76:77], v[76:77], v[4:5] op_sel_hi:[1,0]
	v_pk_mul_f32 v[74:75], v[74:75], v[4:5] op_sel_hi:[1,0]
	v_pk_mul_f32 v[72:73], v[72:73], v[4:5] op_sel_hi:[1,0]
	v_pk_mul_f32 v[70:71], v[70:71], v[4:5] op_sel_hi:[1,0]
	v_mov_b32_e32 v4, v143
	v_pk_mul_f32 v[52:53], v[52:53], v[4:5] op_sel_hi:[1,0]
	v_pk_mul_f32 v[50:51], v[50:51], v[4:5] op_sel_hi:[1,0]
	v_pk_mul_f32 v[48:49], v[48:49], v[4:5] op_sel_hi:[1,0]
	v_pk_mul_f32 v[46:47], v[46:47], v[4:5] op_sel_hi:[1,0]
	v_pk_mul_f32 v[44:45], v[44:45], v[4:5] op_sel_hi:[1,0]
	v_pk_mul_f32 v[42:43], v[42:43], v[4:5] op_sel_hi:[1,0]
	v_pk_mul_f32 v[40:41], v[40:41], v[4:5] op_sel_hi:[1,0]
	v_pk_mul_f32 v[38:39], v[38:39], v[4:5] op_sel_hi:[1,0]
	v_mov_b32_e32 v4, v145
	v_pk_mul_f32 v[100:101], v[100:101], v[140:141] op_sel_hi:[1,0]
	v_pk_mul_f32 v[98:99], v[98:99], v[140:141] op_sel_hi:[1,0]
	v_pk_mul_f32 v[96:97], v[96:97], v[140:141] op_sel_hi:[1,0]
	v_pk_mul_f32 v[94:95], v[94:95], v[140:141] op_sel_hi:[1,0]
	v_pk_mul_f32 v[92:93], v[92:93], v[140:141] op_sel_hi:[1,0]
	v_pk_mul_f32 v[90:91], v[90:91], v[140:141] op_sel_hi:[1,0]
	v_pk_mul_f32 v[88:89], v[88:89], v[140:141] op_sel_hi:[1,0]
	v_pk_mul_f32 v[86:87], v[86:87], v[140:141] op_sel_hi:[1,0]
	v_pk_mul_f32 v[68:69], v[68:69], v[142:143] op_sel_hi:[1,0]
	v_pk_mul_f32 v[66:67], v[66:67], v[142:143] op_sel_hi:[1,0]
	v_pk_mul_f32 v[64:65], v[64:65], v[142:143] op_sel_hi:[1,0]
	v_pk_mul_f32 v[62:63], v[62:63], v[142:143] op_sel_hi:[1,0]
	v_pk_mul_f32 v[60:61], v[60:61], v[142:143] op_sel_hi:[1,0]
	v_pk_mul_f32 v[58:59], v[58:59], v[142:143] op_sel_hi:[1,0]
	v_pk_mul_f32 v[56:57], v[56:57], v[142:143] op_sel_hi:[1,0]
	v_pk_mul_f32 v[54:55], v[54:55], v[142:143] op_sel_hi:[1,0]
	v_pk_mul_f32 v[36:37], v[36:37], v[144:145] op_sel_hi:[1,0]
	v_pk_mul_f32 v[34:35], v[34:35], v[144:145] op_sel_hi:[1,0]
	v_pk_mul_f32 v[32:33], v[32:33], v[144:145] op_sel_hi:[1,0]
	v_pk_mul_f32 v[30:31], v[30:31], v[144:145] op_sel_hi:[1,0]
	v_pk_mul_f32 v[28:29], v[28:29], v[144:145] op_sel_hi:[1,0]
	v_pk_mul_f32 v[26:27], v[26:27], v[144:145] op_sel_hi:[1,0]
	v_pk_mul_f32 v[24:25], v[24:25], v[144:145] op_sel_hi:[1,0]
	v_pk_mul_f32 v[22:23], v[22:23], v[144:145] op_sel_hi:[1,0]
	v_pk_mul_f32 v[20:21], v[20:21], v[4:5] op_sel_hi:[1,0]
	v_pk_mul_f32 v[18:19], v[18:19], v[4:5] op_sel_hi:[1,0]
	v_pk_mul_f32 v[16:17], v[16:17], v[4:5] op_sel_hi:[1,0]
	v_pk_mul_f32 v[14:15], v[14:15], v[4:5] op_sel_hi:[1,0]
	v_pk_mul_f32 v[12:13], v[12:13], v[4:5] op_sel_hi:[1,0]
	v_pk_mul_f32 v[10:11], v[10:11], v[4:5] op_sel_hi:[1,0]
	v_pk_mul_f32 v[8:9], v[8:9], v[4:5] op_sel_hi:[1,0]
	v_pk_mul_f32 v[6:7], v[6:7], v[4:5] op_sel_hi:[1,0]
	s_branch .LBB0_711

	.amdhsa_kernel _Z3fwd4Args
		.amdhsa_group_segment_fixed_size 0
		.amdhsa_private_segment_fixed_size 0
		.amdhsa_kernarg_size 472
		.amdhsa_user_sgpr_count 2
		.amdhsa_user_sgpr_dispatch_ptr 0
		.amdhsa_user_sgpr_queue_ptr 0
		.amdhsa_user_sgpr_kernarg_segment_ptr 1
		.amdhsa_user_sgpr_dispatch_id 0
		.amdhsa_user_sgpr_kernarg_preload_length 0
		.amdhsa_user_sgpr_kernarg_preload_offset 0
		.amdhsa_user_sgpr_private_segment_size 0
		.amdhsa_uses_dynamic_stack 0
		.amdhsa_enable_private_segment 0
		.amdhsa_system_sgpr_workgroup_id_x 1
		.amdhsa_system_sgpr_workgroup_id_y 0
		.amdhsa_system_sgpr_workgroup_id_z 0
		.amdhsa_system_sgpr_workgroup_info 0
		.amdhsa_system_vgpr_workitem_id 0
		.amdhsa_next_free_vgpr 256
		.amdhsa_next_free_sgpr 98
		.amdhsa_accum_offset 256
		.amdhsa_reserve_vcc 1
		.amdhsa_float_round_mode_32 0
		.amdhsa_float_round_mode_16_64 0
		.amdhsa_float_denorm_mode_32 3
		.amdhsa_float_denorm_mode_16_64 3
		.amdhsa_dx10_clamp 1
		.amdhsa_ieee_mode 1
		.amdhsa_fp16_overflow 0
		.amdhsa_tg_split 0
		.amdhsa_exception_fp_ieee_invalid_op 0
		.amdhsa_exception_fp_denorm_src 0
		.amdhsa_exception_fp_ieee_div_zero 0
		.amdhsa_exception_fp_ieee_overflow 0
		.amdhsa_exception_fp_ieee_underflow 0
		.amdhsa_exception_fp_ieee_inexact 0
		.amdhsa_exception_int_div_zero 0
	.end_amdhsa_kernel

amdhsa.kernels:
  - .agpr_count:     0
    .args:
      - .offset:         0
        .size:           216
        .value_kind:     by_value
      - .offset:         216
        .size:           4
        .value_kind:     hidden_block_count_x
      - .offset:         220
        .size:           4
        .value_kind:     hidden_block_count_y
      - .offset:         224
        .size:           4
        .value_kind:     hidden_block_count_z
      - .offset:         228
        .size:           2
        .value_kind:     hidden_group_size_x
      - .offset:         230
        .size:           2
        .value_kind:     hidden_group_size_y
      - .offset:         232
        .size:           2
        .value_kind:     hidden_group_size_z
      - .offset:         234
        .size:           2
        .value_kind:     hidden_remainder_x
      - .offset:         236
        .size:           2
        .value_kind:     hidden_remainder_y
      - .offset:         238
        .size:           2
        .value_kind:     hidden_remainder_z
      - .offset:         256
        .size:           8
        .value_kind:     hidden_global_offset_x
      - .offset:         264
        .size:           8
        .value_kind:     hidden_global_offset_y
      - .offset:         272
        .size:           8
        .value_kind:     hidden_global_offset_z
      - .offset:         280
        .size:           2
        .value_kind:     hidden_grid_dims
      - .offset:         336
        .size:           4
        .value_kind:     hidden_dynamic_lds_size
    .group_segment_fixed_size: 0
    .kernarg_segment_align: 8
    .kernarg_segment_size: 472
    .language:       OpenCL C
    .language_version:
      - 2
      - 0
    .max_flat_workgroup_size: 512
    .name:           _Z3fwd4Args
    .private_segment_fixed_size: 0
    .sgpr_count:     104
    .sgpr_spill_count: 68
    .symbol:         _Z3fwd4Args.kd
    .uniform_work_group_size: 1
    .uses_dynamic_stack: false
    .vgpr_count:     256
    .vgpr_spill_count: 0
    .wavefront_size: 64
